# P10 combine loop software-pipelined: next row's x and 12 of 16 expert-output loads issued before the current row's arithmetic and stores
# baseline (speedup 1.0000x reference)
; __global__ void __launch_bounds__(NTHREADS, 2) mk_fwd(Args args) {
;     ...
;     if (IN(10)) {
;         const int gw = F.vcu * NWAVES + F.wave, NGW = F.G * NWAVES;
;         const bf16_t* X2 = WSP(bf16_t, WS_X2); const unsigned char* Y = WSP(unsigned char, WS_Y);
;         f32x4 gfin[4][2];
; #pragma unroll
;         for (int j = 0; j < 4; ++j)
; #pragma unroll
;             for (int h = 0; h < 2; ++h) gfin[j][h] = *(const f32x4*)(F.g_final + 8 * F.lane + 512 * j + 4 * h);
;         for (int m = gw; m < NTOK; m += NGW) {
;             const bf16_t* xr = X2 + (size_t)m * DM + 8 * F.lane;
;             f32x4 v[4][2]; float s = 0.f; u32x4 xw[4];
; #pragma unroll
;             for (int j = 0; j < 4; ++j) xw[j] = *(const u32x4*)(xr + 512 * j);
;             u32x2 yw[4][4];
; #pragma unroll
;             for (int k = 0; k < 4; ++k)
; #pragma unroll
;                 for (int j = 0; j < 4; ++j) yw[k][j] = *(const u32x2*)(Y + (size_t)(m * 4 + k) * DM + 8 * F.lane + 512 * j);
.LBB0_1402:
	s_cmp_lt_i32 s86, 11
	s_cselect_b64 s[2:3], -1, 0
	s_and_b64 s[0:1], s[2:3], s[0:1]
	s_andn2_b64 vcc, exec, s[0:1]
	s_cbranch_vccnz .LBB0_1406
	s_lshl_b32 s0, s52, 3
	s_add_i32 s2, s0, s25
	s_cmpk_gt_i32 s2, 0x3fff
	s_cbranch_scc1 .LBB0_1406
	v_readlane_b32 s4, v254, 0
	s_waitcnt vmcnt(0)
	v_mov_b32_e32 v33, 0
	v_readlane_b32 s6, v254, 2
	v_readlane_b32 s7, v254, 3
	v_readlane_b32 s10, v254, 6
	v_readlane_b32 s11, v254, 7
	v_lshlrev_b32_e32 v34, 5, v190
	v_mov_b32_e32 v35, v33
	s_mov_b64 s[6:7], s[10:11]
	v_lshl_add_u64 v[24:25], s[6:7], 0, v[34:35]
	s_movk_i32 s3, 0x1000
	v_readlane_b32 s5, v254, 1
	s_waitcnt lgkmcnt(0)
	global_load_dwordx4 v[0:3], v34, s[10:11] offset:16
	global_load_dwordx4 v[4:7], v34, s[10:11]
	global_load_dwordx4 v[8:11], v34, s[10:11] offset:2064
	global_load_dwordx4 v[12:15], v34, s[10:11] offset:2048
	s_mov_b64 s[0:1], 0x1000
	v_add_co_u32_e32 v36, vcc, s3, v24
	v_lshl_add_u64 v[26:27], v[24:25], 0, s[0:1]
	s_nop 0
	v_addc_co_u32_e32 v37, vcc, 0, v25, vcc
	s_mov_b64 s[4:5], 0x1800
	global_load_dwordx4 v[16:19], v[36:37], off
	global_load_dwordx4 v[20:23], v[26:27], off offset:16
	v_lshl_add_u64 v[38:39], v[24:25], 0, s[4:5]
	global_load_dwordx4 v[24:27], v[36:37], off offset:2048
	global_load_dwordx4 v[28:31], v[38:39], off offset:16
	v_lshlrev_b32_e32 v32, 3, v190
	v_lshl_add_u64 v[36:37], s[30:31], 0, v[32:33]
	v_mbcnt_lo_u32_b32 v32, -1, 0
	s_mov_b64 s[6:7], 0x72000000
	v_mbcnt_hi_u32_b32 v32, -1, v32
	v_lshl_add_u64 v[48:49], v[36:37], 0, s[6:7]
	v_and_b32_e32 v36, 64, v32
	v_add_u32_e32 v36, 64, v36
	v_xor_b32_e32 v37, 1, v32
	v_cmp_lt_i32_e32 vcc, v37, v36
	s_ashr_i32 s3, s2, 31
	s_lshl_b32 s4, s33, 3
	v_cndmask_b32_e32 v37, v32, v37, vcc
	v_lshlrev_b32_e32 v54, 2, v37
	v_xor_b32_e32 v37, 2, v32
	v_cmp_lt_i32_e32 vcc, v37, v36
	s_lshl_b64 s[6:7], s[2:3], 12
	s_add_u32 s6, s30, s6
	v_cndmask_b32_e32 v37, v32, v37, vcc
	v_lshlrev_b32_e32 v55, 2, v37
	v_xor_b32_e32 v37, 4, v32
	v_cmp_lt_i32_e32 vcc, v37, v36
	s_addc_u32 s7, s31, s7
	v_readlane_b32 s8, v254, 4
	v_cndmask_b32_e32 v37, v32, v37, vcc
	v_lshlrev_b32_e32 v56, 2, v37
	v_xor_b32_e32 v37, 8, v32
	v_cmp_lt_i32_e32 vcc, v37, v36
	v_readlane_b32 s9, v254, 5
	s_ashr_i32 s5, s4, 31
	v_cndmask_b32_e32 v37, v32, v37, vcc
	v_lshlrev_b32_e32 v57, 2, v37
	v_xor_b32_e32 v37, 16, v32
	v_cmp_lt_i32_e32 vcc, v37, v36
	s_lshl_b64 s[8:9], s[2:3], 13
	v_mov_b32_e32 v60, 0x3727c5ac
	v_cndmask_b32_e32 v37, v32, v37, vcc
	v_lshlrev_b32_e32 v58, 2, v37
	v_xor_b32_e32 v37, 32, v32
	v_cmp_lt_i32_e32 vcc, v37, v36
	v_mov_b32_e32 v61, 0x260
	s_nop 0
	v_cndmask_b32_e32 v32, v32, v37, vcc
	v_lshlrev_b32_e32 v59, 2, v32
	v_lshlrev_b32_e32 v32, 4, v190
	v_lshl_add_u64 v[32:33], s[6:7], 0, v[32:33]
	s_mov_b64 s[6:7], 0x24000000
	v_lshl_add_u64 v[50:51], v[32:33], 0, s[6:7]
	s_lshl_b64 s[6:7], s[4:5], 12
	s_add_u32 s8, s28, s8
	s_addc_u32 s9, s29, s9
	v_lshl_add_u64 v[32:33], s[8:9], 0, v[34:35]
	v_lshl_add_u64 v[52:53], v[32:33], 0, s[0:1]
	s_lshl_b32 s0, s52, 5
	s_lshl_b32 s1, s25, 2
	s_lshl_b64 s[8:9], s[4:5], 13
	s_add_i32 s10, s0, s1
	s_lshl_b32 s3, s33, 5
	s_mov_b32 s5, 0xf800000
	s_mov_b32 s21, s10
	global_load_dwordx4 v[218:221], v[50:51], off
	global_load_dwordx4 v[214:217], v[50:51], off offset:1024
	global_load_dwordx4 v[210:213], v[50:51], off offset:2048
	global_load_dwordx4 v[206:209], v[50:51], off offset:3072
	s_mov_b32 s34, s21
	s_ashr_i32 s35, s34, 31
	s_lshl_b64 s[36:37], s[34:35], 11
	v_lshl_add_u64 v[246:247], v[48:49], 0, s[36:37]
	global_load_dwordx2 v[222:223], v[246:247], off
	global_load_dwordx2 v[224:225], v[246:247], off offset:512
	global_load_dwordx2 v[226:227], v[246:247], off offset:1024
	global_load_dwordx2 v[228:229], v[246:247], off offset:1536
	s_add_i32 s34, s21, 1
	s_ashr_i32 s35, s34, 31
	s_lshl_b64 s[36:37], s[34:35], 11
	v_lshl_add_u64 v[248:249], v[48:49], 0, s[36:37]
	global_load_dwordx2 v[230:231], v[248:249], off
	global_load_dwordx2 v[232:233], v[248:249], off offset:512
	global_load_dwordx2 v[234:235], v[248:249], off offset:1024
	global_load_dwordx2 v[236:237], v[248:249], off offset:1536
	s_add_i32 s34, s21, 2
	s_ashr_i32 s35, s34, 31
	s_lshl_b64 s[36:37], s[34:35], 11
	v_lshl_add_u64 v[250:251], v[48:49], 0, s[36:37]
	global_load_dwordx2 v[238:239], v[250:251], off
	global_load_dwordx2 v[240:241], v[250:251], off offset:512
	global_load_dwordx2 v[242:243], v[250:251], off offset:1024
	global_load_dwordx2 v[244:245], v[250:251], off offset:1536
	s_waitcnt vmcnt(0)
	s_branch .Lp10_go
.LBB0_1405:
	s_waitcnt vmcnt(8)
; __global__ void __launch_bounds__(NTHREADS, 2) mk_fwd(Args args) {
;     ...
;         for (int m = gw; m < NTOK; m += NGW) {
;             const bf16_t* xr = X2 + (size_t)m * DM + 8 * F.lane;
;             f32x4 v[4][2]; float s = 0.f; u32x4 xw[4];
; #pragma unroll
;             for (int j = 0; j < 4; ++j) xw[j] = *(const u32x4*)(xr + 512 * j);
;             u32x2 yw[4][4];
; #pragma unroll
;             for (int k = 0; k < 4; ++k)
; #pragma unroll
;                 for (int j = 0; j < 4; ++j) yw[k][j] = *(const u32x2*)(Y + (size_t)(m * 4 + k) * DM + 8 * F.lane + 512 * j);
; #pragma unroll
;             for (int j = 0; j < 4; ++j) { v[j][0] = (f32x4){bf_lo(xw[j].x), bf_hi(xw[j].x), bf_lo(xw[j].y), bf_hi(xw[j].y)}; v[j][1] = (f32x4){bf_lo(xw[j].z), bf_hi(xw[j].z), bf_lo(xw[j].w), bf_hi(xw[j].w)}; }
; #pragma unroll
;             for (int k = 0; k < 4; ++k)
; #pragma unroll
;                 for (int j = 0; j < 4; ++j) { const f32x2 a = __builtin_amdgcn_cvt_pk_f32_fp8((int)yw[k][j].x, false), b2 = __builtin_amdgcn_cvt_pk_f32_fp8((int)yw[k][j].x, true),
;                         c = __builtin_amdgcn_cvt_pk_f32_fp8((int)yw[k][j].y, false), d = __builtin_amdgcn_cvt_pk_f32_fp8((int)yw[k][j].y, true);
;                     v[j][0] += (f32x4){a.x, a.y, b2.x, b2.y}; v[j][1] += (f32x4){c.x, c.y, d.x, d.y}; }
.Lp10_go:
	v_mov_b64_e32 v[32:33], v[206:207]
	v_mov_b64_e32 v[34:35], v[208:209]
	v_mov_b64_e32 v[36:37], v[210:211]
	v_mov_b64_e32 v[38:39], v[212:213]
	v_mov_b64_e32 v[40:41], v[214:215]
	v_mov_b64_e32 v[42:43], v[216:217]
	v_mov_b64_e32 v[44:45], v[218:219]
	v_mov_b64_e32 v[46:47], v[220:221]
	v_mov_b64_e32 v[64:65], v[222:223]
	v_mov_b64_e32 v[66:67], v[224:225]
	v_mov_b64_e32 v[68:69], v[226:227]
	v_mov_b64_e32 v[70:71], v[228:229]
	v_mov_b64_e32 v[76:77], v[230:231]
	v_mov_b64_e32 v[78:79], v[232:233]
	v_mov_b64_e32 v[80:81], v[234:235]
	v_mov_b64_e32 v[82:83], v[236:237]
	v_mov_b64_e32 v[84:85], v[238:239]
	v_mov_b64_e32 v[86:87], v[240:241]
	v_mov_b64_e32 v[88:89], v[242:243]
	v_mov_b64_e32 v[90:91], v[244:245]
	s_add_i32 s34, s10, 3
	s_ashr_i32 s35, s34, 31
	s_lshl_b64 s[36:37], s[34:35], 11
	v_lshl_add_u64 v[252:253], v[48:49], 0, s[36:37]
	global_load_dwordx2 v[92:93], v[252:253], off
	global_load_dwordx2 v[94:95], v[252:253], off offset:512
	global_load_dwordx2 v[96:97], v[252:253], off offset:1024
	global_load_dwordx2 v[98:99], v[252:253], off offset:1536
	s_add_i32 s2, s2, s4
	s_add_i32 s21, s10, s3
	s_cmpk_lt_i32 s2, 0x4000
	s_cselect_b32 s20, 1, 0
	s_cselect_b32 s21, s21, s10
	s_cselect_b32 s38, s6, 0
	s_cselect_b32 s39, s7, 0
	s_add_i32 s10, s10, s3
	v_lshl_add_u64 v[50:51], v[50:51], 0, s[38:39]
	global_load_dwordx4 v[218:221], v[50:51], off
	global_load_dwordx4 v[214:217], v[50:51], off offset:1024
	global_load_dwordx4 v[210:213], v[50:51], off offset:2048
	global_load_dwordx4 v[206:209], v[50:51], off offset:3072
	s_mov_b32 s34, s21
	s_ashr_i32 s35, s34, 31
	s_lshl_b64 s[36:37], s[34:35], 11
	v_lshl_add_u64 v[246:247], v[48:49], 0, s[36:37]
	global_load_dwordx2 v[222:223], v[246:247], off
	global_load_dwordx2 v[224:225], v[246:247], off offset:512
	global_load_dwordx2 v[226:227], v[246:247], off offset:1024
	global_load_dwordx2 v[228:229], v[246:247], off offset:1536
	s_add_i32 s34, s21, 1
	s_ashr_i32 s35, s34, 31
	s_lshl_b64 s[36:37], s[34:35], 11
	v_lshl_add_u64 v[248:249], v[48:49], 0, s[36:37]
	global_load_dwordx2 v[230:231], v[248:249], off
	global_load_dwordx2 v[232:233], v[248:249], off offset:512
	global_load_dwordx2 v[234:235], v[248:249], off offset:1024
	global_load_dwordx2 v[236:237], v[248:249], off offset:1536
	s_add_i32 s34, s21, 2
	s_ashr_i32 s35, s34, 31
	s_lshl_b64 s[36:37], s[34:35], 11
	v_lshl_add_u64 v[250:251], v[48:49], 0, s[36:37]
	global_load_dwordx2 v[238:239], v[250:251], off
	global_load_dwordx2 v[240:241], v[250:251], off offset:512
	global_load_dwordx2 v[242:243], v[250:251], off offset:1024
	global_load_dwordx2 v[244:245], v[250:251], off offset:1536
	s_nop 0
	v_lshlrev_b32_e32 v62, 16, v44
	s_nop 0
	v_cvt_pk_f32_fp8_e32 v[110:111], v64
	v_cvt_pk_f32_fp8_sdwa v[112:113], v64 src0_sel:WORD_1
	v_cvt_pk_f32_fp8_e32 v[114:115], v65
	v_cvt_pk_f32_fp8_sdwa v[64:65], v65 src0_sel:WORD_1
	s_nop 0
	v_cvt_pk_f32_fp8_e32 v[116:117], v66
	v_cvt_pk_f32_fp8_sdwa v[118:119], v66 src0_sel:WORD_1
	s_nop 0
	v_cvt_pk_f32_fp8_e32 v[128:129], v70
	v_cvt_pk_f32_fp8_sdwa v[130:131], v70 src0_sel:WORD_1
	v_cvt_pk_f32_fp8_e32 v[132:133], v71
	v_cvt_pk_f32_fp8_sdwa v[70:71], v71 src0_sel:WORD_1
	s_nop 0
	v_cvt_pk_f32_fp8_e32 v[134:135], v76
	v_cvt_pk_f32_fp8_sdwa v[136:137], v76 src0_sel:WORD_1
	v_cvt_pk_f32_fp8_e32 v[138:139], v77
	v_cvt_pk_f32_fp8_sdwa v[76:77], v77 src0_sel:WORD_1
	s_nop 0
	v_cvt_pk_f32_fp8_e32 v[140:141], v78
	v_cvt_pk_f32_fp8_sdwa v[142:143], v78 src0_sel:WORD_1
	s_nop 0
	v_cvt_pk_f32_fp8_e32 v[158:159], v84
	v_cvt_pk_f32_fp8_sdwa v[160:161], v84 src0_sel:WORD_1
	v_cvt_pk_f32_fp8_e32 v[162:163], v85
	v_cvt_pk_f32_fp8_sdwa v[84:85], v85 src0_sel:WORD_1
	v_and_b32_e32 v63, 0xffff0000, v44
	v_lshlrev_b32_e32 v44, 16, v45
	v_and_b32_e32 v45, 0xffff0000, v45
	v_lshlrev_b32_e32 v72, 16, v46
	v_and_b32_e32 v73, 0xffff0000, v46
	v_lshlrev_b32_e32 v46, 16, v47
	v_and_b32_e32 v47, 0xffff0000, v47
	v_cvt_pk_f32_fp8_e32 v[120:121], v67
	v_cvt_pk_f32_fp8_sdwa v[66:67], v67 src0_sel:WORD_1
	v_cvt_pk_f32_fp8_e32 v[122:123], v68
	v_cvt_pk_f32_fp8_sdwa v[124:125], v68 src0_sel:WORD_1
	v_cvt_pk_f32_fp8_e32 v[126:127], v69
	v_cvt_pk_f32_fp8_sdwa v[68:69], v69 src0_sel:WORD_1
	s_nop 0
	v_cvt_pk_f32_fp8_e32 v[164:165], v86
	v_cvt_pk_f32_fp8_sdwa v[166:167], v86 src0_sel:WORD_1
	s_waitcnt vmcnt(19)
	v_cvt_pk_f32_fp8_e32 v[182:183], v92
	v_cvt_pk_f32_fp8_sdwa v[184:185], v92 src0_sel:WORD_1
	v_cvt_pk_f32_fp8_e32 v[186:187], v93
	v_cvt_pk_f32_fp8_sdwa v[92:93], v93 src0_sel:WORD_1
	v_lshlrev_b32_e32 v74, 16, v40
	v_and_b32_e32 v75, 0xffff0000, v40
	v_lshlrev_b32_e32 v40, 16, v41
	v_and_b32_e32 v41, 0xffff0000, v41
	v_lshlrev_b32_e32 v108, 16, v34
	v_and_b32_e32 v109, 0xffff0000, v34
	v_lshlrev_b32_e32 v34, 16, v35
	v_and_b32_e32 v35, 0xffff0000, v35
	v_cvt_pk_f32_fp8_e32 v[144:145], v79
	v_cvt_pk_f32_fp8_sdwa v[78:79], v79 src0_sel:WORD_1
	v_cvt_pk_f32_fp8_e32 v[146:147], v80
	v_cvt_pk_f32_fp8_sdwa v[148:149], v80 src0_sel:WORD_1
	v_cvt_pk_f32_fp8_e32 v[150:151], v81
	v_cvt_pk_f32_fp8_sdwa v[80:81], v81 src0_sel:WORD_1
	s_waitcnt vmcnt(18)
; __global__ void __launch_bounds__(NTHREADS, 2) mk_fwd(Args args) {
;     ...
;             for (int j = 0; j < 4; ++j) { v[j][0] = (f32x4){bf_lo(xw[j].x), bf_hi(xw[j].x), bf_lo(xw[j].y), bf_hi(xw[j].y)}; v[j][1] = (f32x4){bf_lo(xw[j].z), bf_hi(xw[j].z), bf_lo(xw[j].w), bf_hi(xw[j].w)}; }
; #pragma unroll
;             for (int k = 0; k < 4; ++k)
; #pragma unroll
;                 for (int j = 0; j < 4; ++j) { const f32x2 a = __builtin_amdgcn_cvt_pk_f32_fp8((int)yw[k][j].x, false), b2 = __builtin_amdgcn_cvt_pk_f32_fp8((int)yw[k][j].x, true),
;                         c = __builtin_amdgcn_cvt_pk_f32_fp8((int)yw[k][j].y, false), d = __builtin_amdgcn_cvt_pk_f32_fp8((int)yw[k][j].y, true);
;                     v[j][0] += (f32x4){a.x, a.y, b2.x, b2.y}; v[j][1] += (f32x4){c.x, c.y, d.x, d.y}; }
; #pragma unroll
;             for (int j = 0; j < 4; ++j)
; #pragma unroll
;                 for (int h = 0; h < 2; ++h) s += (v[j][h].x * v[j][h].x + v[j][h].y * v[j][h].y) + (v[j][h].z * v[j][h].z + v[j][h].w * v[j][h].w);
	v_cvt_pk_f32_fp8_e32 v[188:189], v94
	v_cvt_pk_f32_fp8_sdwa v[190:191], v94 src0_sel:WORD_1
	v_pk_add_f32 v[62:63], v[110:111], v[62:63]
	v_pk_add_f32 v[44:45], v[112:113], v[44:45]
	v_pk_add_f32 v[72:73], v[114:115], v[72:73]
	v_pk_add_f32 v[46:47], v[64:65], v[46:47]
	v_cvt_pk_f32_fp8_e32 v[152:153], v82
	v_cvt_pk_f32_fp8_sdwa v[154:155], v82 src0_sel:WORD_1
	v_cvt_pk_f32_fp8_e32 v[156:157], v83
	v_cvt_pk_f32_fp8_sdwa v[82:83], v83 src0_sel:WORD_1
	v_cvt_pk_f32_fp8_e32 v[168:169], v87
	v_cvt_pk_f32_fp8_sdwa v[86:87], v87 src0_sel:WORD_1
	v_cvt_pk_f32_fp8_e32 v[170:171], v88
	v_cvt_pk_f32_fp8_sdwa v[172:173], v88 src0_sel:WORD_1
	v_cvt_pk_f32_fp8_e32 v[174:175], v89
	v_cvt_pk_f32_fp8_sdwa v[88:89], v89 src0_sel:WORD_1
	v_pk_add_f32 v[40:41], v[118:119], v[40:41]
	v_pk_add_f32 v[64:65], v[116:117], v[74:75]
	v_pk_add_f32 v[34:35], v[70:71], v[34:35]
	v_pk_add_f32 v[44:45], v[136:137], v[44:45]
	v_pk_add_f32 v[62:63], v[134:135], v[62:63]
	v_pk_add_f32 v[46:47], v[76:77], v[46:47]
	v_pk_add_f32 v[70:71], v[138:139], v[72:73]
	v_lshlrev_b32_e32 v100, 16, v42
	v_and_b32_e32 v101, 0xffff0000, v42
	v_lshlrev_b32_e32 v42, 16, v43
	v_and_b32_e32 v43, 0xffff0000, v43
	v_lshlrev_b32_e32 v104, 16, v38
	v_and_b32_e32 v105, 0xffff0000, v38
	v_lshlrev_b32_e32 v38, 16, v39
	v_and_b32_e32 v39, 0xffff0000, v39
	v_cvt_pk_f32_fp8_e32 v[192:193], v95
	v_cvt_pk_f32_fp8_sdwa v[94:95], v95 src0_sel:WORD_1
	v_pk_add_f32 v[64:65], v[140:141], v[64:65]
	v_pk_add_f32 v[40:41], v[142:143], v[40:41]
	v_pk_add_f32 v[62:63], v[158:159], v[62:63]
	v_pk_add_f32 v[44:45], v[160:161], v[44:45]
	v_pk_add_f32 v[70:71], v[162:163], v[70:71]
	v_pk_add_f32 v[46:47], v[84:85], v[46:47]
	v_lshlrev_b32_e32 v102, 16, v36
	v_and_b32_e32 v103, 0xffff0000, v36
	v_lshlrev_b32_e32 v36, 16, v37
	v_and_b32_e32 v37, 0xffff0000, v37
	v_cvt_pk_f32_fp8_e32 v[176:177], v90
	v_cvt_pk_f32_fp8_sdwa v[178:179], v90 src0_sel:WORD_1
	v_cvt_pk_f32_fp8_e32 v[180:181], v91
	v_cvt_pk_f32_fp8_sdwa v[90:91], v91 src0_sel:WORD_1
	s_waitcnt vmcnt(17)
	v_cvt_pk_f32_fp8_e32 v[194:195], v96
	v_cvt_pk_f32_fp8_sdwa v[196:197], v96 src0_sel:WORD_1
	v_pk_add_f32 v[74:75], v[120:121], v[100:101]
	v_pk_add_f32 v[42:43], v[66:67], v[42:43]
	v_pk_add_f32 v[38:39], v[68:69], v[38:39]
	v_pk_add_f32 v[40:41], v[166:167], v[40:41]
	v_pk_add_f32 v[64:65], v[164:165], v[64:65]
	v_pk_add_f32 v[44:45], v[184:185], v[44:45]
	v_pk_add_f32 v[62:63], v[182:183], v[62:63]
	v_pk_add_f32 v[46:47], v[92:93], v[46:47]
	v_pk_add_f32 v[70:71], v[186:187], v[70:71]
	v_cvt_pk_f32_fp8_e32 v[198:199], v97
	v_cvt_pk_f32_fp8_sdwa v[96:97], v97 src0_sel:WORD_1
	v_pk_add_f32 v[66:67], v[122:123], v[102:103]
	v_pk_add_f32 v[36:37], v[124:125], v[36:37]
	v_pk_add_f32 v[42:43], v[78:79], v[42:43]
	v_pk_add_f32 v[72:73], v[144:145], v[74:75]
	v_pk_add_f32 v[38:39], v[80:81], v[38:39]
	v_pk_add_f32 v[64:65], v[188:189], v[64:65]
	v_pk_add_f32 v[40:41], v[190:191], v[40:41]
	v_mov_b32_e32 v80, v63
	v_mov_b32_e32 v81, v71
	v_mov_b32_e32 v84, v45
	v_mov_b32_e32 v85, v47
	v_pk_add_f32 v[68:69], v[126:127], v[104:105]
	v_pk_add_f32 v[102:103], v[132:133], v[108:109]
	v_pk_add_f32 v[36:37], v[148:149], v[36:37]
	v_pk_add_f32 v[66:67], v[146:147], v[66:67]
	v_pk_add_f32 v[34:35], v[82:83], v[34:35]
	v_pk_add_f32 v[72:73], v[168:169], v[72:73]
	v_pk_add_f32 v[42:43], v[86:87], v[42:43]
	v_pk_add_f32 v[38:39], v[88:89], v[38:39]
	v_mov_b32_e32 v78, v62
	v_mov_b32_e32 v79, v70
	v_mov_b32_e32 v82, v44
	v_mov_b32_e32 v83, v46
	v_pk_mul_f32 v[86:87], v[40:41], v[40:41]
	v_pk_mul_f32 v[88:89], v[64:65], v[64:65]
	v_pk_mul_f32 v[80:81], v[80:81], v[80:81]
	v_pk_mul_f32 v[84:85], v[84:85], v[84:85]
	v_lshlrev_b32_e32 v106, 16, v32
	v_and_b32_e32 v107, 0xffff0000, v32
	v_lshlrev_b32_e32 v32, 16, v33
	v_and_b32_e32 v33, 0xffff0000, v33
	s_waitcnt vmcnt(16)
; __device__ __forceinline__ float wave_sum(float v) {
; #pragma unroll
;     for (int o = 1; o < 64; o <<= 1) v += __shfl_xor(v, o);
;     return v;
; __global__ void __launch_bounds__(NTHREADS, 2) mk_fwd(Args args) {
;     ...
; #pragma unroll
;             for (int j = 0; j < 4; ++j)
; #pragma unroll
;                 for (int h = 0; h < 2; ++h) s += (v[j][h].x * v[j][h].x + v[j][h].y * v[j][h].y) + (v[j][h].z * v[j][h].z + v[j][h].w * v[j][h].w);
;             s = wave_sum(s);
;             const float rstd = 1.0f / sqrtf(s * (1.0f / DM) + RMS_EPS);
;             float* orow = F.out + (size_t)m * DM + 8 * F.lane;
; #pragma unroll
;             for (int j = 0; j < 4; ++j)
; #pragma unroll
;                 for (int h = 0; h < 2; ++h) *(f32x4*)(orow + 512 * j + 4 * h) = v[j][h] * rstd * gfin[j][h];
	v_cvt_pk_f32_fp8_e32 v[200:201], v98
	v_cvt_pk_f32_fp8_sdwa v[202:203], v98 src0_sel:WORD_1
	v_pk_add_f32 v[68:69], v[150:151], v[68:69]
	v_pk_add_f32 v[76:77], v[156:157], v[102:103]
	v_pk_add_f32 v[66:67], v[170:171], v[66:67]
	v_pk_add_f32 v[36:37], v[172:173], v[36:37]
	v_pk_add_f32 v[42:43], v[94:95], v[42:43]
	v_pk_add_f32 v[72:73], v[192:193], v[72:73]
	v_pk_mov_b32 v[102:103], v[88:89], v[86:87] op_sel:[1,0]
	v_mov_b32_e32 v89, v87
	v_pk_fma_f32 v[78:79], v[78:79], v[78:79], v[80:81]
	v_pk_fma_f32 v[80:81], v[82:83], v[82:83], v[84:85]
	v_cvt_pk_f32_fp8_e32 v[204:205], v99
	v_cvt_pk_f32_fp8_sdwa v[98:99], v99 src0_sel:WORD_1
	v_pk_add_f32 v[100:101], v[128:129], v[106:107]
	v_pk_add_f32 v[32:33], v[130:131], v[32:33]
	v_pk_add_f32 v[68:69], v[174:175], v[68:69]
	v_pk_add_f32 v[34:35], v[90:91], v[34:35]
	v_pk_add_f32 v[36:37], v[196:197], v[36:37]
	v_pk_add_f32 v[66:67], v[194:195], v[66:67]
	v_mul_f32_e32 v90, v73, v73
	v_mul_f32_e32 v92, v43, v43
	v_pk_add_f32 v[82:83], v[102:103], v[88:89]
	v_pk_add_f32 v[78:79], v[78:79], v[80:81]
	v_pk_add_f32 v[32:33], v[154:155], v[32:33]
	v_pk_add_f32 v[74:75], v[152:153], v[100:101]
	v_pk_add_f32 v[68:69], v[198:199], v[68:69]
	v_pk_add_f32 v[38:39], v[96:97], v[38:39]
	v_mul_f32_e32 v101, v66, v66
	v_mul_f32_e32 v104, v67, v67
	v_mul_f32_e32 v105, v36, v36
	v_mul_f32_e32 v106, v37, v37
	v_pk_fma_f32 v[86:87], v[72:73], v[72:73], v[90:91] op_sel_hi:[1,1,0]
	v_pk_fma_f32 v[90:91], v[42:43], v[42:43], v[92:93] op_sel_hi:[1,1,0]
	v_pk_add_f32 v[80:81], v[82:83], v[82:83] op_sel:[0,1] op_sel_hi:[1,0]
	v_pk_add_f32 v[78:79], v[78:79], v[78:79] op_sel:[0,1] op_sel_hi:[1,0]
	v_pk_add_f32 v[74:75], v[176:177], v[74:75]
	v_pk_add_f32 v[32:33], v[178:179], v[32:33]
	v_pk_mul_f32 v[94:95], v[38:39], v[38:39]
	v_pk_mul_f32 v[96:97], v[68:69], v[68:69]
	v_mov_b32_e32 v87, v105
	v_mov_b32_e32 v91, v106
	v_mov_b32_e32 v81, v104
	v_mov_b32_e32 v79, v101
	v_pk_add_f32 v[76:77], v[180:181], v[76:77]
	v_pk_add_f32 v[32:33], v[202:203], v[32:33]
	v_pk_add_f32 v[74:75], v[200:201], v[74:75]
	v_pk_mov_b32 v[92:93], v[96:97], v[94:95] op_sel:[1,0]
	v_mov_b32_e32 v97, v95
	v_pk_add_f32 v[82:83], v[86:87], v[90:91]
	v_pk_add_f32 v[78:79], v[78:79], v[80:81]
	v_pk_add_f32 v[34:35], v[98:99], v[34:35]
	v_pk_add_f32 v[76:77], v[204:205], v[76:77]
	v_mul_f32_e32 v98, v75, v75
	v_mul_f32_e32 v100, v33, v33
	v_pk_add_f32 v[84:85], v[92:93], v[96:97]
	v_pk_add_f32 v[78:79], v[78:79], v[82:83]
	v_mul_f32_e32 v107, v76, v76
	v_mul_f32_e32 v108, v77, v77
	v_mul_f32_e32 v109, v34, v34
	v_mul_f32_e32 v110, v35, v35
	v_pk_fma_f32 v[94:95], v[74:75], v[74:75], v[98:99] op_sel_hi:[1,1,0]
	v_pk_fma_f32 v[98:99], v[32:33], v[32:33], v[100:101] op_sel_hi:[1,1,0]
	v_pk_add_f32 v[84:85], v[84:85], v[84:85] op_sel:[0,1] op_sel_hi:[1,0]
	v_pk_add_f32 v[78:79], v[78:79], v[78:79] op_sel:[0,1] op_sel_hi:[1,0]
	v_mov_b32_e32 v95, v109
	v_mov_b32_e32 v99, v110
	v_mov_b32_e32 v85, v108
	v_mov_b32_e32 v79, v107
	v_pk_add_f32 v[86:87], v[94:95], v[98:99]
	v_pk_add_f32 v[78:79], v[78:79], v[84:85]
	s_nop 0
	v_pk_add_f32 v[78:79], v[78:79], v[86:87]
	s_nop 0
	v_add_f32_e32 v78, v78, v79
	ds_bpermute_b32 v79, v54, v78
	s_waitcnt lgkmcnt(0)
	v_add_f32_e32 v78, v78, v79
	ds_bpermute_b32 v79, v55, v78
	s_waitcnt lgkmcnt(0)
	v_add_f32_e32 v78, v78, v79
	ds_bpermute_b32 v79, v56, v78
	s_waitcnt lgkmcnt(0)
	v_add_f32_e32 v78, v78, v79
	ds_bpermute_b32 v79, v57, v78
	s_waitcnt lgkmcnt(0)
	v_add_f32_e32 v78, v78, v79
	ds_bpermute_b32 v79, v58, v78
	s_waitcnt lgkmcnt(0)
	v_add_f32_e32 v78, v78, v79
	ds_bpermute_b32 v79, v59, v78
	s_waitcnt lgkmcnt(0)
	v_add_f32_e32 v78, v78, v79
	v_fmamk_f32 v78, v78, 0x3a000000, v60
	v_mul_f32_e32 v79, 0x4f800000, v78
	v_cmp_gt_f32_e32 vcc, s5, v78
	s_nop 1
	v_cndmask_b32_e32 v78, v78, v79, vcc
	v_sqrt_f32_e32 v79, v78
	s_nop 0
	v_add_u32_e32 v80, -1, v79
	v_add_u32_e32 v81, 1, v79
	v_fma_f32 v82, -v80, v79, v78
	v_fma_f32 v83, -v81, v79, v78
	v_cmp_ge_f32_e64 s[0:1], 0, v82
	s_nop 1
	v_cndmask_b32_e64 v79, v79, v80, s[0:1]
	v_cmp_lt_f32_e64 s[0:1], 0, v83
	s_nop 1
	v_cndmask_b32_e64 v79, v79, v81, s[0:1]
	v_mul_f32_e32 v80, 0x37800000, v79
	v_cndmask_b32_e32 v79, v79, v80, vcc
	v_cmp_class_f32_e32 vcc, v78, v61
	s_nop 1
	v_cndmask_b32_e32 v78, v79, v78, vcc
	v_div_scale_f32 v79, s[0:1], v78, v78, 1.0
	v_rcp_f32_e32 v81, v79
	v_div_scale_f32 v80, vcc, 1.0, v78, 1.0
	v_fma_f32 v82, -v79, v81, 1.0
	v_fmac_f32_e32 v81, v82, v81
	v_mul_f32_e32 v82, v80, v81
	v_fma_f32 v83, -v79, v82, v80
	v_fmac_f32_e32 v82, v83, v81
	v_fma_f32 v79, -v79, v82, v80
	v_div_fmas_f32 v79, v79, v81, v82
	v_div_fixup_f32 v78, v79, v78, 1.0
	v_pk_mul_f32 v[62:63], v[78:79], v[62:63] op_sel_hi:[0,1]
	v_pk_mul_f32 v[44:45], v[78:79], v[44:45] op_sel_hi:[0,1]
	v_pk_mul_f32 v[70:71], v[78:79], v[70:71] op_sel_hi:[0,1]
	v_pk_mul_f32 v[46:47], v[78:79], v[46:47] op_sel_hi:[0,1]
	v_pk_mul_f32 v[64:65], v[78:79], v[64:65] op_sel_hi:[0,1]
	v_pk_mul_f32 v[40:41], v[78:79], v[40:41] op_sel_hi:[0,1]
	v_pk_mul_f32 v[72:73], v[78:79], v[72:73] op_sel_hi:[0,1]
	v_pk_mul_f32 v[80:81], v[78:79], v[42:43] op_sel_hi:[0,1]
	v_pk_mul_f32 v[66:67], v[78:79], v[66:67] op_sel_hi:[0,1]
	v_pk_mul_f32 v[82:83], v[78:79], v[36:37] op_sel_hi:[0,1]
	v_pk_mul_f32 v[84:85], v[78:79], v[68:69] op_sel_hi:[0,1]
	v_pk_mul_f32 v[68:69], v[78:79], v[38:39] op_sel_hi:[0,1]
	v_pk_mul_f32 v[74:75], v[78:79], v[74:75] op_sel_hi:[0,1]
	v_pk_mul_f32 v[86:87], v[78:79], v[32:33] op_sel_hi:[0,1]
	v_pk_mul_f32 v[88:89], v[78:79], v[76:77] op_sel_hi:[0,1]
	v_pk_mul_f32 v[76:77], v[78:79], v[34:35] op_sel_hi:[0,1]
	v_pk_mul_f32 v[34:35], v[44:45], v[6:7]
	v_pk_mul_f32 v[32:33], v[62:63], v[4:5]
	v_pk_mul_f32 v[38:39], v[46:47], v[2:3]
	v_pk_mul_f32 v[36:37], v[70:71], v[0:1]
	v_pk_mul_f32 v[42:43], v[40:41], v[14:15]
	v_pk_mul_f32 v[40:41], v[64:65], v[12:13]
	v_pk_mul_f32 v[46:47], v[80:81], v[10:11]
	v_pk_mul_f32 v[44:45], v[72:73], v[8:9]
	v_pk_mul_f32 v[64:65], v[82:83], v[18:19]
	v_pk_mul_f32 v[62:63], v[66:67], v[16:17]
	v_pk_mul_f32 v[68:69], v[68:69], v[22:23]
	v_pk_mul_f32 v[66:67], v[84:85], v[20:21]
	v_pk_mul_f32 v[72:73], v[86:87], v[26:27]
	v_pk_mul_f32 v[70:71], v[74:75], v[24:25]
	v_pk_mul_f32 v[76:77], v[76:77], v[30:31]
	v_pk_mul_f32 v[74:75], v[88:89], v[28:29]
	global_store_dwordx4 v[52:53], v[32:35], off offset:-4096
	global_store_dwordx4 v[52:53], v[36:39], off offset:-4080
	global_store_dwordx4 v[52:53], v[40:43], off offset:-2048
	global_store_dwordx4 v[52:53], v[44:47], off offset:-2032
	global_store_dwordx4 v[52:53], v[62:65], off
	global_store_dwordx4 v[52:53], v[66:69], off offset:16
	global_store_dwordx4 v[52:53], v[70:73], off offset:2048
	global_store_dwordx4 v[52:53], v[74:77], off offset:2064
	v_lshl_add_u64 v[52:53], v[52:53], 0, s[8:9]
	s_cmp_lg_u32 s20, 0
	s_cbranch_scc1 .LBB0_1405
